# gate/up grouped GEMM: per-unit token-list load wait deferred to the end of the first K iteration (loads into free VGPRs)
# baseline (speedup 1.0000x reference)
; #define PG8_STAGE(bufoff, gbase, v0, v1) do { \
;         __builtin_amdgcn_global_load_lds((const unsigned*)((const char*)(gbase) + (v0)), (LAS unsigned*)(lds + (bufoff) + ldsw), 16, 0, 0); \
;         __builtin_amdgcn_global_load_lds((const unsigned*)((const char*)(gbase) + (v1)), (LAS unsigned*)(lds + (bufoff) + ldsw + 8192), 16, 0, 0); } while (0)
; #define PG8_WAIT_V(n) asm volatile("s_waitcnt vmcnt(" #n ")" ::: "memory")
; #define PG8_BAR __builtin_amdgcn_s_barrier()
; #define PG8_AOFFS(u, o00, o01, o10, o11) do { S.a_off4(u, R0, R1, o00, o01, o10, o11); o00 += (unsigned)C0 * 2u; o01 += (unsigned)C1 * 2u; o10 += (unsigned)C0 * 2u; o11 += (unsigned)C1 * 2u; } while (0)
;     __device__ __forceinline__ const char* b_ptr(const Unit& u) const { return (const char*)(Bt + (size_t)u.pn * BM * K); }
;     __device__ __forceinline__ const char* b_ptr(const Unit& u) const { return (const char*)(W + (size_t)u.e * 1024 * D + (size_t)u.pn * BM * 8); }
;     __device__ __forceinline__ const char* b_ptr(const Unit& u) const { return (const char*)(W + (size_t)u.e * D * FF + (size_t)u.pn * BM * 8); }
; template <class Epi, class Sched>
; __device__ __forceinline__ void gemm_phase(LAS unsigned char* lds, const int K, const Sched& S, const Epi& E) {
;     ...
;     PG8_AOFFS(cur, c00, c01, c10, c11);
;     const char* cB = S.b_ptr(cur);
;     PG8_STAGE(PG8_SB(0, 0), cB, voffB0, voffB1); PG8_STAGE(PG8_SA(0, 0), gA, c00, c01); PG8_STAGE(PG8_SB(0, 1), cB + hstep, voffB0, voffB1); PG8_STAGE(PG8_SA(0, 1), gA, c10, c11);
;     if (wr == 1) PG8_BAR;
;     PG8_WAIT_V(4); PG8_BAR;
;     PG8_STAGE(PG8_SB(1, 0), cB + kstepB, voffB0, voffB1); PG8_STAGE(PG8_SA(1, 0), gA + kstep, c00, c01); PG8_STAGE(PG8_SB(1, 1), cB + hstep + kstepB, voffB0, voffB1);
;     PG8_WAIT_V(6); PG8_BAR;
.LBB0_1084:
	s_lshl_b32 s7, s8, 8
	s_cmp_lt_i32 s6, 64
	s_cselect_b64 vcc, -1, 0
	s_add_u32 s6, s0, 0x3ee90000
	v_mov_b32_e32 v5, s7
	s_addc_u32 s7, s1, 0
	s_add_u32 s8, s0, 0x34c30080
	s_addc_u32 s9, s1, 0
	s_lshl_b32 s11, s11, 5
	s_and_b32 s11, s11, 0x60
	s_lshl_b32 s14, s10, 13
	s_lshl_b32 s15, s11, 7
	s_add_u32 s12, s20, 0x20000
	s_addc_u32 s13, s21, 0
	v_lshl_add_u64 v[2:3], s[12:13], 0, v[130:131]
	s_add_i32 m0, s37, 0x18000
	s_waitcnt vmcnt(4)
	s_barrier
	global_load_lds_dwordx4 v[2:3], off
	v_lshl_add_u64 v[2:3], s[12:13], 0, v[132:133]
	s_add_i32 m0, s37, 0x1a000
	s_add_i32 s43, s37, 0x8000
	s_add_i32 s44, s37, 0xa000
	global_load_lds_dwordx4 v[2:3], off
	v_lshl_add_u64 v[2:3], s[8:9], 0, v[134:135]
	s_mov_b32 m0, s43
	s_add_u32 s12, s20, 0x20800
	global_load_lds_dwordx4 v[2:3], off
	v_lshl_add_u64 v[2:3], s[8:9], 0, v[136:137]
	s_mov_b32 m0, s44
	s_addc_u32 s13, s21, 0
	global_load_lds_dwordx4 v[2:3], off
	v_lshl_add_u64 v[2:3], s[12:13], 0, v[130:131]
	s_add_i32 m0, s37, 0x1c000
	v_add_u32_e32 v4, 0xff00, v7
	global_load_lds_dwordx4 v[2:3], off
	v_lshl_add_u64 v[2:3], s[12:13], 0, v[132:133]
	s_add_i32 m0, s37, 0x1e000
	v_cndmask_b32_e32 v157, v4, v5, vcc
	global_load_lds_dwordx4 v[2:3], off
	v_lshrrev_b32_e32 v3, 1, v6
	v_and_b32_e32 v3, 24, v3
	v_and_b32_e32 v2, 15, v6
	v_lshlrev_b32_e32 v4, 1, v3
	v_lshl_or_b32 v137, s10, 6, v2
	v_lshl_or_b32 v2, v2, 6, v4
	v_lshlrev_b32_e32 v4, 2, v6
	v_and_b32_e32 v4, 32, v4
	s_waitcnt vmcnt(6)
	v_bitop3_b32 v5, v2, s14, v4 bitop3:0xde
	v_bitop3_b32 v149, v2, s15, v4 bitop3:0xde
	s_mov_b32 s45, 0x8000
	v_or_b32_e32 v150, s11, v3
	s_add_i32 s46, 0, 0x10000
	v_add_u32_e32 v151, 0, v5
	s_mov_b32 s47, 0xc000
	s_add_i32 s48, 0, 0x14000
	s_mov_b64 s[10:11], 0x80
	s_mov_b32 s49, 0x20000
	s_mov_b32 s50, 0x24000
	s_mov_b32 s51, 0x28000
	v_readlane_b32 s53, v254, 27
	v_mov_b32_e32 v158, v134
	s_barrier
	s_mov_b32 s91, 0

; #define PG8_AOFFS(u, o00, o01, o10, o11) do { S.a_off4(u, R0, R1, o00, o01, o10, o11); o00 += (unsigned)C0 * 2u; o01 += (unsigned)C1 * 2u; o10 += (unsigned)C0 * 2u; o11 += (unsigned)C1 * 2u; } while (0)
;     __device__ __forceinline__ void a_off4(const Unit& u, int r0, int r1, unsigned& o00, unsigned& o01, unsigned& o10, unsigned& o11) const { o00 = a_off(u, r0); o01 = a_off(u, r1); o10 = a_off(u, HALF + r0); o11 = a_off(u, HALF + r1); }
;     __device__ __forceinline__ const char* b_ptr(const Unit& u) const { return (const char*)(Bt + (size_t)u.pn * BM * K); }
;     __device__ __forceinline__ const char* b_ptr(const Unit& u) const { return (const char*)(W + (size_t)u.e * 1024 * D + (size_t)u.pn * BM * 8); }
;     __device__ __forceinline__ void a_off4(const Unit& u, int r0, int r1, unsigned& o00, unsigned& o01, unsigned& o10, unsigned& o11) const { o00 = a_off(u, r0); o01 = a_off(u, r1); o10 = a_off(u, HALF + r0); o11 = a_off(u, HALF + r1); }
;     __device__ __forceinline__ const char* b_ptr(const Unit& u) const { return (const char*)(W + (size_t)u.e * D * FF + (size_t)u.pn * BM * 8); }
; template <class Epi, class Sched>
; __device__ __forceinline__ void gemm_phase(LAS unsigned char* lds, const int K, const Sched& S, const Epi& E) {
;     ...
;         const bool has_next = S.next(ui + 1, nxt);
;         const char* nB = cB;
;         if (has_next) { PG8_AOFFS(nxt, n00, n01, n10, n11); nB = S.b_ptr(nxt); } else { n00 = c00; n01 = c01; n10 = c10; n11 = c11; }
;     __device__ __forceinline__ void a_off4(const Unit& u, int r0, int r1, unsigned& o00, unsigned& o01, unsigned& o10, unsigned& o11) const {
;         const int p0 = u.pm * BM + r0, p1 = u.pm * BM + r1, p2 = p0 + HALF, p3 = p1 + HALF;
;         if (u.e >= NE) { o00 = (unsigned)p0 * (unsigned)(D * 2); o01 = (unsigned)p1 * (unsigned)(D * 2); o10 = (unsigned)p2 * (unsigned)(D * 2); o11 = (unsigned)p3 * (unsigned)(D * 2); return; }
;         const int* lp = list + u.e * T;
;         int v0 = lp[p0], v1 = lp[p1], v2 = lp[p2], v3 = lp[p3];
;         asm volatile("" : "+v"(v0), "+v"(v1), "+v"(v2), "+v"(v3));
;         const int c = cnt[u.e];
;         o00 = p0 < c ? (unsigned)v0 * (unsigned)(D * 2) : 0u; o01 = p1 < c ? (unsigned)v1 * (unsigned)(D * 2) : 0u;
;         o10 = p2 < c ? (unsigned)v2 * (unsigned)(D * 2) : 0u; o11 = p3 < c ? (unsigned)v3 * (unsigned)(D * 2) : 0u;
.LBB0_1087:
	s_andn2_b64 vcc, exec, s[18:19]
	s_mov_b64 s[18:19], s[20:21]
	v_mov_b32_e32 v153, v140
	v_mov_b32_e32 v154, v138
	v_mov_b32_e32 v155, v136
	v_mov_b32_e32 v156, v158
	s_cbranch_vccnz .LBB0_1093
	s_lshl_b32 s13, s52, 8
	v_add_u32_e32 v2, s13, v1
	v_add_u32_e32 v4, s13, v146
	v_add_u32_e32 v6, 0x80, v2
	v_add_u32_e32 v7, 0x80, v4
	s_cmp_lt_i32 s14, 64
	s_mov_b64 s[18:19], -1
	s_cbranch_scc0 .LBB0_1090
	s_lshl_b32 s18, s14, 13
	s_ashr_i32 s19, s18, 31
	s_lshl_b64 s[18:19], s[18:19], 2
	s_add_u32 s18, s31, s18
	s_addc_u32 s19, s33, s19
	v_ashrrev_i32_e32 v3, 31, v2
	v_ashrrev_i32_e32 v5, 31, v4
	v_lshl_add_u64 v[8:9], v[2:3], 2, s[18:19]
	v_lshl_add_u64 v[10:11], v[4:5], 2, s[18:19]
	global_load_dword v232, v[8:9], off
	global_load_dword v233, v[10:11], off
	s_nop 0
	global_load_dword v234, v[10:11], off offset:512
	s_nop 0
	global_load_dword v235, v[8:9], off offset:512
	s_lshl_b32 s92, s52, 8
	s_mov_b32 s93, s14
	s_mov_b32 s91, 1
	s_mov_b64 s[18:19], 0

; #define PG8_AOFFS(u, o00, o01, o10, o11) do { S.a_off4(u, R0, R1, o00, o01, o10, o11); o00 += (unsigned)C0 * 2u; o01 += (unsigned)C1 * 2u; o10 += (unsigned)C0 * 2u; o11 += (unsigned)C1 * 2u; } while (0)
;     __device__ __forceinline__ const char* b_ptr(const Unit& u) const { return (const char*)(Bt + (size_t)u.pn * BM * K); }
;     __device__ __forceinline__ const char* b_ptr(const Unit& u) const { return (const char*)(W + (size_t)u.e * 1024 * D + (size_t)u.pn * BM * 8); }
;     __device__ __forceinline__ const char* b_ptr(const Unit& u) const { return (const char*)(W + (size_t)u.e * D * FF + (size_t)u.pn * BM * 8); }
; template <class Epi, class Sched>
; __device__ __forceinline__ void gemm_phase(LAS unsigned char* lds, const int K, const Sched& S, const Epi& E) {
;     ...
;         if (has_next) { PG8_AOFFS(nxt, n00, n01, n10, n11); nB = S.b_ptr(nxt); } else { n00 = c00; n01 = c01; n10 = c10; n11 = c11; }
;     __device__ __forceinline__ void a_off4(const Unit& u, int r0, int r1, unsigned& o00, unsigned& o01, unsigned& o10, unsigned& o11) const {
;     ...
;         const int c = cnt[u.e];
;         o00 = p0 < c ? (unsigned)v0 * (unsigned)(D * 2) : 0u; o01 = p1 < c ? (unsigned)v1 * (unsigned)(D * 2) : 0u;
;         o10 = p2 < c ? (unsigned)v2 * (unsigned)(D * 2) : 0u; o11 = p3 < c ? (unsigned)v3 * (unsigned)(D * 2) : 0u;
.Lpb8_p8j:
	s_cmp_eq_u32 s91, 0
	s_cbranch_scc1 .Lgl_g0_skip
	s_mov_b32 s91, 0
	s_lshl_b32 s94, s93, 2
	s_add_i32 s94, s94, 0x21660
	v_mov_b32_e32 v236, s94
	ds_read_b32 v236, v236
	v_add_u32_e32 v237, s92, v1
	v_lshlrev_b32_e32 v232, 12, v232
	v_lshlrev_b32_e32 v233, 12, v233
	v_lshlrev_b32_e32 v234, 12, v234
	v_lshlrev_b32_e32 v235, 12, v235
	s_waitcnt lgkmcnt(0)
	v_cmp_lt_i32_e64 s[94:95], v237, v236
	v_add_u32_e32 v237, 0x80, v237
	s_nop 1
	v_cndmask_b32_e64 v232, 0, v232, s[94:95]
	v_cmp_lt_i32_e64 s[96:97], v237, v236
	v_add_u32_e32 v237, s92, v146
	s_nop 1
	v_cndmask_b32_e64 v235, 0, v235, s[96:97]
	v_cmp_lt_i32_e64 s[94:95], v237, v236
	v_add_u32_e32 v237, 0x80, v237
	s_nop 1
	v_cndmask_b32_e64 v233, 0, v233, s[94:95]
	v_cmp_lt_i32_e64 s[96:97], v237, v236
	v_add_u32_e32 v156, v232, v147
	v_add_u32_e32 v154, v235, v147
	v_cndmask_b32_e64 v234, 0, v234, s[96:97]
	v_add_u32_e32 v155, v233, v148
	v_add_u32_e32 v153, v234, v148

; #define PG8_STAGE(bufoff, gbase, v0, v1) do { \
;         __builtin_amdgcn_global_load_lds((const unsigned*)((const char*)(gbase) + (v0)), (LAS unsigned*)(lds + (bufoff) + ldsw), 16, 0, 0); \
;         __builtin_amdgcn_global_load_lds((const unsigned*)((const char*)(gbase) + (v1)), (LAS unsigned*)(lds + (bufoff) + ldsw + 8192), 16, 0, 0); } while (0)
; #define PG8_WAIT_V(n) asm volatile("s_waitcnt vmcnt(" #n ")" ::: "memory")
; #define PG8_BAR __builtin_amdgcn_s_barrier()
; #define PG8_AOFFS(u, o00, o01, o10, o11) do { S.a_off4(u, R0, R1, o00, o01, o10, o11); o00 += (unsigned)C0 * 2u; o01 += (unsigned)C1 * 2u; o10 += (unsigned)C0 * 2u; o11 += (unsigned)C1 * 2u; } while (0)
;     __device__ __forceinline__ const char* b_ptr(const Unit& u) const { return (const char*)(Bt + (size_t)u.pn * BM * K); }
;     __device__ __forceinline__ const char* b_ptr(const Unit& u) const { return (const char*)(W + (size_t)u.e * 1024 * D + (size_t)u.pn * BM * 8); }
;     __device__ __forceinline__ const char* b_ptr(const Unit& u) const { return (const char*)(W + (size_t)u.e * D * FF + (size_t)u.pn * BM * 8); }
; template <class Epi, class Sched>
; __device__ __forceinline__ void gemm_phase(LAS unsigned char* lds, const int K, const Sched& S, const Epi& E) {
;     ...
;     PG8_AOFFS(cur, c00, c01, c10, c11);
;     const char* cB = S.b_ptr(cur);
;     PG8_STAGE(PG8_SB(0, 0), cB, voffB0, voffB1); PG8_STAGE(PG8_SA(0, 0), gA, c00, c01); PG8_STAGE(PG8_SB(0, 1), cB + hstep, voffB0, voffB1); PG8_STAGE(PG8_SA(0, 1), gA, c10, c11);
;     if (wr == 1) PG8_BAR;
;     PG8_WAIT_V(4); PG8_BAR;
;     PG8_STAGE(PG8_SB(1, 0), cB + kstepB, voffB0, voffB1); PG8_STAGE(PG8_SA(1, 0), gA + kstep, c00, c01); PG8_STAGE(PG8_SB(1, 1), cB + hstep + kstepB, voffB0, voffB1);
;     PG8_WAIT_V(6); PG8_BAR;
.LBB0_1821:
	s_lshl_b32 s7, s8, 8
	s_cmp_lt_i32 s6, 64
	s_cselect_b64 vcc, -1, 0
	s_add_u32 s6, s0, 0x3ee90000
	v_mov_b32_e32 v5, s7
	s_addc_u32 s7, s1, 0
	s_add_u32 s8, s0, 0x34c30080
	s_addc_u32 s9, s1, 0
	s_lshl_b32 s11, s11, 5
	s_and_b32 s11, s11, 0x60
	s_lshl_b32 s14, s10, 13
	s_lshl_b32 s15, s11, 7
	s_add_u32 s12, s20, 0x20000
	s_addc_u32 s13, s21, 0
	v_lshl_add_u64 v[2:3], s[12:13], 0, v[130:131]
	s_add_i32 m0, s37, 0x18000
	s_waitcnt vmcnt(4)
	s_barrier
	global_load_lds_dwordx4 v[2:3], off
	v_lshl_add_u64 v[2:3], s[12:13], 0, v[132:133]
	s_add_i32 m0, s37, 0x1a000
	s_add_i32 s43, s37, 0x8000
	s_add_i32 s44, s37, 0xa000
	global_load_lds_dwordx4 v[2:3], off
	v_lshl_add_u64 v[2:3], s[8:9], 0, v[134:135]
	s_mov_b32 m0, s43
	s_add_u32 s12, s20, 0x20800
	global_load_lds_dwordx4 v[2:3], off
	v_lshl_add_u64 v[2:3], s[8:9], 0, v[136:137]
	s_mov_b32 m0, s44
	s_addc_u32 s13, s21, 0
	global_load_lds_dwordx4 v[2:3], off
	v_lshl_add_u64 v[2:3], s[12:13], 0, v[130:131]
	s_add_i32 m0, s37, 0x1c000
	v_add_u32_e32 v4, 0xff00, v7
	global_load_lds_dwordx4 v[2:3], off
	v_lshl_add_u64 v[2:3], s[12:13], 0, v[132:133]
	s_add_i32 m0, s37, 0x1e000
	v_cndmask_b32_e32 v157, v4, v5, vcc
	global_load_lds_dwordx4 v[2:3], off
	v_lshrrev_b32_e32 v3, 1, v6
	v_and_b32_e32 v3, 24, v3
	v_and_b32_e32 v2, 15, v6
	v_lshlrev_b32_e32 v4, 1, v3
	v_lshl_or_b32 v137, s10, 6, v2
	v_lshl_or_b32 v2, v2, 6, v4
	v_lshlrev_b32_e32 v4, 2, v6
	v_and_b32_e32 v4, 32, v4
	s_waitcnt vmcnt(6)
	v_bitop3_b32 v5, v2, s14, v4 bitop3:0xde
	v_bitop3_b32 v149, v2, s15, v4 bitop3:0xde
	s_mov_b32 s45, 0x8000
	v_or_b32_e32 v150, s11, v3
	s_add_i32 s46, 0, 0x10000
	v_add_u32_e32 v151, 0, v5
	s_mov_b32 s47, 0xc000
	s_add_i32 s48, 0, 0x14000
	s_mov_b64 s[10:11], 0x80
	s_mov_b32 s49, 0x20000
	s_mov_b32 s50, 0x24000
	s_mov_b32 s51, 0x28000
	v_mov_b32_e32 v158, v134
	s_barrier
	s_mov_b32 s91, 0
